# s25
# speedup vs baseline: 1.0120x; 1.0120x over previous
.LBB1_7:
	s_or_b64 exec, exec, s[0:1]
	v_lshl_add_u64 v[254:255], v[252:253], 0, s[58:59]
	s_add_u32 m0, s32, 0x2000
	s_nop 0
	global_load_lds_dwordx4 v[254:255], off
	s_setprio 1
	s_waitcnt lgkmcnt(0)
	v_mfma_f32_16x16x32_f16 v[24:27], v[152:155], v[134:137], v[24:27]
	v_mfma_f32_16x16x32_f16 v[44:47], v[152:155], v[138:141], v[44:47]
	v_mfma_f32_16x16x32_f16 v[172:175], v[156:159], v[142:145], v[64:67]
	v_mfma_f32_16x16x32_f16 v[66:69], v[156:159], v[148:151], v[68:71]
	v_mfma_f32_16x16x32_f16 v[160:163], v[152:155], v[142:145], v[48:51]
	v_mfma_f32_16x16x32_f16 v[152:155], v[152:155], v[148:151], v[52:55]
	v_mfma_f32_16x16x32_f16 v[164:167], v[156:159], v[134:137], v[56:59]
	v_mfma_f32_16x16x32_f16 v[168:171], v[156:159], v[138:141], v[60:63]
	s_setprio 0
	ds_read_b128 v[48:51], v129 offset:40960
	ds_read_b128 v[52:55], v129 offset:43008
	v_lshl_add_u64 v[254:255], v[252:253], 0, s[60:61]
	s_add_u32 m0, s32, 0x4000
	s_nop 0
	global_load_lds_dwordx4 v[254:255], off
	s_setprio 1
	s_waitcnt lgkmcnt(0)
	v_mfma_f32_16x16x32_f16 v[28:31], v[48:51], v[134:137], v[28:31]
	v_mfma_f32_16x16x32_f16 v[70:73], v[48:51], v[138:141], v[72:75]
	v_mfma_f32_16x16x32_f16 v[74:77], v[48:51], v[142:145], v[76:79]
	v_mfma_f32_16x16x32_f16 v[78:81], v[48:51], v[148:151], v[80:83]
	v_mfma_f32_16x16x32_f16 v[82:85], v[52:55], v[134:137], v[84:87]
	v_mfma_f32_16x16x32_f16 v[86:89], v[52:55], v[138:141], v[88:91]
	v_mfma_f32_16x16x32_f16 v[90:93], v[52:55], v[142:145], v[92:95]
	v_mfma_f32_16x16x32_f16 v[94:97], v[52:55], v[148:151], v[96:99]
	s_setprio 0
	ds_read_b128 v[48:51], v129 offset:45056
	ds_read_b128 v[52:55], v129 offset:47104
	v_lshl_add_u64 v[254:255], v[252:253], 0, s[62:63]
	s_add_u32 m0, s32, 0x6000
	s_nop 0
	global_load_lds_dwordx4 v[254:255], off
	s_setprio 1
	s_waitcnt lgkmcnt(0)
	v_mfma_f32_16x16x32_f16 v[202:205], v[52:55], v[138:141], v[116:119]
	v_mfma_f32_16x16x32_f16 v[206:209], v[52:55], v[142:145], v[120:123]
	v_mfma_f32_16x16x32_f16 v[156:159], v[48:51], v[134:137], v[32:35]
	v_mfma_f32_16x16x32_f16 v[176:179], v[48:51], v[138:141], v[100:103]
	v_mfma_f32_16x16x32_f16 v[180:183], v[48:51], v[142:145], v[104:107]
	v_mfma_f32_16x16x32_f16 v[184:187], v[48:51], v[148:151], v[108:111]
	v_mfma_f32_16x16x32_f16 v[188:191], v[52:55], v[134:137], v[112:115]
	v_mfma_f32_16x16x32_f16 v[148:151], v[52:55], v[148:151], v[124:127]
	s_setprio 0
	ds_read_b128 v[210:213], v128 offset:32768
	ds_read_b128 v[214:217], v128 offset:34816
	ds_read_b128 v[218:221], v128 offset:36864
	ds_read_b128 v[222:225], v128 offset:38912
	ds_read_b128 v[32:35], v130 offset:32768
	ds_read_b128 v[98:101], v130 offset:34816
	s_mov_b64 s[100:101], 0x8000
	v_lshl_add_u64 v[254:255], v[252:253], 0, s[100:101]
	s_add_u32 m0, s32, 0x10000
	s_nop 0
	global_load_lds_dwordx4 v[254:255], off
	s_setprio 1
	s_waitcnt lgkmcnt(0)
	v_mfma_f32_16x16x32_f16 v[50:53], v[32:35], v[210:213], v[0:3]
	v_mfma_f32_16x16x32_f16 v[54:57], v[32:35], v[214:217], v[4:7]
	v_mfma_f32_16x16x32_f16 v[58:61], v[32:35], v[218:221], v[8:11]
	v_mfma_f32_16x16x32_f16 v[62:65], v[32:35], v[222:225], v[12:15]
	v_mfma_f32_16x16x32_f16 v[142:145], v[98:101], v[210:213], v[16:19]
	v_mfma_f32_16x16x32_f16 v[138:141], v[98:101], v[214:217], v[20:23]
	v_mfma_f32_16x16x32_f16 v[134:137], v[98:101], v[218:221], v[36:39]
	v_mfma_f32_16x16x32_f16 v[126:129], v[98:101], v[222:225], v[40:43]
	s_setprio 0
	ds_read_b128 v[0:3], v130 offset:36864
	ds_read_b128 v[4:7], v130 offset:38912
	s_mov_b64 s[100:101], 0xa000
	v_lshl_add_u64 v[254:255], v[252:253], 0, s[100:101]
	s_add_u32 m0, s32, 0x12000
	s_nop 0
	global_load_lds_dwordx4 v[254:255], off
	s_setprio 1
	s_waitcnt lgkmcnt(0)
	v_mfma_f32_16x16x32_f16 v[34:37], v[0:3], v[210:213], v[24:27]
	v_mfma_f32_16x16x32_f16 v[38:41], v[0:3], v[214:217], v[44:47]
	v_mfma_f32_16x16x32_f16 v[42:45], v[0:3], v[218:221], v[160:163]
	v_mfma_f32_16x16x32_f16 v[46:49], v[0:3], v[222:225], v[152:155]
	v_mfma_f32_16x16x32_f16 v[122:125], v[4:7], v[210:213], v[164:167]
	v_mfma_f32_16x16x32_f16 v[118:121], v[4:7], v[214:217], v[168:171]
	v_mfma_f32_16x16x32_f16 v[114:117], v[4:7], v[218:221], v[172:175]
	v_mfma_f32_16x16x32_f16 v[110:113], v[4:7], v[222:225], v[66:69]
	s_setprio 0
	ds_read_b128 v[10:13], v130 offset:40960
	ds_read_b128 v[18:21], v130 offset:43008
	v_lshl_add_u64 v[254:255], v[252:253], 0, s[66:67]
	s_add_u32 m0, s32, 0x14000
	s_nop 0
	global_load_lds_dwordx4 v[254:255], off
	s_setprio 1
	s_waitcnt lgkmcnt(0)
	v_mfma_f32_16x16x32_f16 v[2:5], v[10:13], v[210:213], v[28:31]
	v_mfma_f32_16x16x32_f16 v[6:9], v[10:13], v[214:217], v[70:73]
	v_mfma_f32_16x16x32_f16 v[14:17], v[10:13], v[218:221], v[74:77]
	v_mfma_f32_16x16x32_f16 v[30:33], v[10:13], v[222:225], v[78:81]
	v_mfma_f32_16x16x32_f16 v[106:109], v[18:21], v[210:213], v[82:85]
	v_mfma_f32_16x16x32_f16 v[102:105], v[18:21], v[214:217], v[86:89]
	v_mfma_f32_16x16x32_f16 v[98:101], v[18:21], v[218:221], v[90:93]
	v_mfma_f32_16x16x32_f16 v[86:89], v[18:21], v[222:225], v[94:97]
	s_setprio 0
	ds_read_b128 v[26:29], v130 offset:45056
	ds_read_b128 v[66:69], v130 offset:47104
	v_lshl_add_u64 v[254:255], v[252:253], 0, s[68:69]
	s_add_u32 m0, s32, 0x16000
	s_nop 0
	global_load_lds_dwordx4 v[254:255], off
	s_setprio 1
	s_waitcnt lgkmcnt(0)
	v_mfma_f32_16x16x32_f16 v[10:13], v[26:29], v[210:213], v[156:159]
	v_mfma_f32_16x16x32_f16 v[18:21], v[26:29], v[214:217], v[176:179]
	v_mfma_f32_16x16x32_f16 v[22:25], v[26:29], v[218:221], v[180:183]
	v_mfma_f32_16x16x32_f16 v[26:29], v[26:29], v[222:225], v[184:187]
	v_mfma_f32_16x16x32_f16 v[78:81], v[66:69], v[210:213], v[188:191]
	v_mfma_f32_16x16x32_f16 v[74:77], v[66:69], v[214:217], v[202:205]
	v_mfma_f32_16x16x32_f16 v[70:73], v[66:69], v[218:221], v[206:209]
	v_mfma_f32_16x16x32_f16 v[66:69], v[66:69], v[222:225], v[148:151]
	s_setprio 0
	s_waitcnt vmcnt(7)
	s_waitcnt lgkmcnt(0)
	s_waitcnt vmcnt(7)
	s_barrier
	v_lshrrev_b32 v0, 4, v194
	s_nop 0
	v_and_b32_e32 v204, 63, v0
	v_lshlrev_b32_e32 v82, 2, v204
	v_ashrrev_i32_e32 v1, 6, v0
	v_cmp_gt_i32_e32 vcc, s82, v0
	v_xor_b32_e32 v205, 0x80, v82
	v_xor_b32_e32 v206, 64, v82
	s_and_saveexec_b64 s[0:1], vcc
	s_cbranch_execz .LBB1_10
	v_sub_f32_e64 v83, v146, |v146|
	v_cmp_eq_u32_e32 vcc, 63, v204
	v_lshlrev_b32_e32 v85, 2, v0
	v_mul_f32_e32 v84, -2.0, v146
	s_nop 1
	v_add_f32_dpp v83, v83, v83 quad_perm:[1,0,3,2] row_mask:0xf bank_mask:0xf
	s_nop 1
	v_add_f32_dpp v83, v83, v83 quad_perm:[2,3,0,1] row_mask:0xf bank_mask:0xf
	s_nop 1
	v_add_f32_dpp v83, v83, v83 row_half_mirror row_mask:0xf bank_mask:0xf
	s_nop 1
	v_add_f32_dpp v83, v83, v83 row_mirror row_mask:0xf bank_mask:0xf
	s_nop 1
	v_add_f32_dpp v83, v83, v83 row_bcast:15 row_mask:0xa bank_mask:0xf
	s_nop 1
	v_add_f32_dpp v83, v83, v83 row_bcast:31 row_mask:0xc bank_mask:0xf
	ds_write2st64_b32 v85, v133, v84 offset0:128 offset1:132
	ds_write_b32 v85, v132 offset:34816
	v_mov_b32_e32 v82, v83
	v_lshlrev_b32_e32 v83, 2, v1
	s_and_b64 exec, exec, vcc
	s_cbranch_execz .LBB1_10
	ds_write_b32 v83, v82 offset:35840
.LBB1_10:
	s_or_b64 exec, exec, s[0:1]
	v_and_b32_e32 v207, 3, v1
	v_and_b32_e32 v174, 15, v0
	v_lshl_or_b32 v175, v207, 6, s75
	s_and_b32 s0, s76, 0x7ffff800
	v_or3_b32 v194, s0, v175, v174
	s_waitcnt lgkmcnt(2)
	v_lshl_add_u64 v[82:83], v[194:195], 2, s[8:9]
	global_load_dword v213, v[82:83], off
	global_load_dword v211, v[82:83], off offset:64
	global_load_dword v210, v[82:83], off offset:128
	global_load_dword v209, v[82:83], off offset:192
	s_waitcnt vmcnt(4)
	s_waitcnt lgkmcnt(0)
	s_barrier
	v_ashrrev_i32_e32 v208, 8, v0
	v_lshlrev_b32_e32 v162, 9, v208
	v_and_or_b32 v176, v204, 48, v162
	ds_read_b128 v[158:161], v176 offset:34816
	ds_read_b128 v[154:157], v176 offset:34880
	ds_read_b128 v[150:153], v176 offset:34944
	ds_read_b128 v[146:149], v176 offset:35008
	ds_read_b128 v[130:133], v176 offset:35072
	ds_read_b128 v[94:97], v176 offset:35136
	ds_read_b128 v[90:93], v176 offset:35200
	ds_read_b128 v[82:85], v176 offset:35264
	v_mad_i32_i24 v164, v208, s83, v162
	ds_read_b64 v[162:163], v164 offset:35840
	s_cmp_eq_u32 s2, 0x1800000
	s_cselect_b64 s[72:73], -1, 0
	s_cmp_lg_u32 s2, 0x1800000
	s_cselect_b64 s[70:71], -1, 0
	v_mov_b32_e32 v202, 0
	s_and_b64 vcc, exec, s[72:73]
	v_mov_b32_e32 v203, 0
	s_cbranch_vccnz .LBB1_12
	s_add_u32 s0, s22, 0x800000
	v_lshlrev_b32_e32 v166, 7, v0
	s_addc_u32 s1, s90, 0
	v_lshlrev_b32_e32 v165, 11, v0
	v_and_b32_e32 v166, 0x80, v166
	s_movk_i32 s64, 0xf000
	v_and_or_b32 v165, v165, s64, v166
	s_add_u32 s80, s22, 0x800100
	global_load_dword v202, v165, s[0:1]
	s_addc_u32 s81, s90, 0
	global_load_dword v203, v165, s[80:81]
